# ssd_out dt stage: 12 dead 64-bit address multiply-adds removed (their loads were hoisted to the item top earlier)
# speedup vs baseline: 1.0018x; 1.0018x over previous
.LBB0_641:
	s_and_b32 s21, s91, 0x1ff
	s_lshl_b32 s20, s21, 6
	v_add_u32_e32 v201, s20, v132
	v_lshlrev_b32_e32 v0, 5, v201
	global_load_dword v0, v0, s[18:19]
	s_nop 0
	global_load_dword v1, v209, s[6:7]
	global_load_dword v2, v209, s[8:9]
	s_mov_b32 s12, 0xbfb8aa3b
	v_add_u32_e32 v3, s20, v141
	v_add_u32_e32 v4, s20, v142
	v_add_u32_e32 v5, s20, v143
	v_add_u32_e32 v6, s20, v144
	v_add_u32_e32 v8, s20, v145
	v_add_u32_e32 v10, s20, v146
	v_add_u32_e32 v12, s20, v147
	v_add_u32_e32 v14, s20, v148
	v_add_u32_e32 v16, s20, v149
	v_add_u32_e32 v17, s20, v150
	v_add_u32_e32 v18, s20, v151
	v_add_u32_e32 v19, s20, v152
	v_mad_i64_i32 v[56:57], s[98:99], v3, s33, v[104:105]
	v_mad_i64_i32 v[60:61], s[98:99], v4, s33, v[106:107]
	v_mad_i64_i32 v[64:65], s[98:99], v5, s33, v[108:109]
	v_mad_i64_i32 v[68:69], s[98:99], v6, s33, v[110:111]
	v_mad_i64_i32 v[72:73], s[98:99], v8, s33, v[112:113]
	v_mad_i64_i32 v[76:77], s[98:99], v10, s33, v[114:115]
	v_mad_i64_i32 v[80:81], s[98:99], v12, s33, v[116:117]
	v_mad_i64_i32 v[84:85], s[98:99], v14, s33, v[118:119]
	v_mad_i64_i32 v[88:89], s[98:99], v16, s33, v[120:121]
	v_mad_i64_i32 v[92:93], s[98:99], v17, s33, v[122:123]
	v_mad_i64_i32 v[96:97], s[98:99], v18, s33, v[124:125]
	v_mad_i64_i32 v[100:101], s[98:99], v19, s33, v[126:127]
	global_load_dwordx4 v[56:59], v[56:57], off
	global_load_dwordx4 v[60:63], v[60:61], off
	global_load_dwordx4 v[64:67], v[64:65], off
	global_load_dwordx4 v[68:71], v[68:69], off
	global_load_dwordx4 v[72:75], v[72:73], off
	global_load_dwordx4 v[76:79], v[76:77], off
	global_load_dwordx4 v[80:83], v[80:81], off
	global_load_dwordx4 v[84:87], v[84:85], off
	global_load_dwordx4 v[88:91], v[88:89], off
	global_load_dwordx4 v[92:95], v[92:93], off
	global_load_dwordx4 v[96:99], v[96:97], off
	global_load_dwordx4 v[100:103], v[100:101], off
	s_waitcnt vmcnt(13)
	v_add_f32_e32 v0, v0, v1
	v_mul_f32_e64 v1, |v0|, s12
	v_exp_f32_e32 v7, v1
	s_waitcnt vmcnt(12)
	s_load_dwordx2 s[98:99], s[92:93], 0x80
	s_waitcnt lgkmcnt(0)
	s_add_u32 s98, s98, s4
	s_addc_u32 s99, s99, s5
	global_load_dword v231, v209, s[98:99]
	v_mul_f32_e32 v1, 0x3fb8aa3b, v2
	v_exp_f32_e32 v9, v1
	v_max_f32_e32 v2, 0, v0
	v_add_f32_e32 v11, 1.0, v7
	v_add_f32_e32 v13, -1.0, v11
	v_frexp_mant_f32_e32 v15, v11
	v_cvt_f64_f32_e32 v[0:1], v11
	s_mov_b32 s12, 0x3f2aaaab
	v_sub_f32_e32 v20, v13, v11
	v_frexp_exp_i32_f64_e32 v0, v[0:1]
	v_cmp_gt_f32_e32 vcc, s12, v15
	v_sub_f32_e32 v13, v7, v13
	v_add_f32_e32 v1, 1.0, v20
	v_subbrev_co_u32_e32 v0, vcc, 0, v0, vcc
	v_add_f32_e32 v1, v13, v1
	v_sub_u32_e32 v13, 0, v0
	v_cvt_f32_i32_e32 v0, v0
	v_ldexp_f32 v11, v11, v13
	v_ldexp_f32 v1, v1, v13
	v_add_f32_e32 v13, -1.0, v11
	v_add_f32_e32 v15, 1.0, v11
	v_add_f32_e32 v20, 1.0, v13
	v_add_f32_e32 v21, -1.0, v15
	v_sub_f32_e32 v20, v11, v20
	v_sub_f32_e32 v11, v11, v21
	v_mul_f32_e32 v21, 0x3f317218, v0
	v_add_f32_e32 v20, v1, v20
	v_add_f32_e32 v1, v1, v11
	s_mov_b32 s12, 0x3f317218
	v_fma_f32 v11, v0, s12, -v21
	v_add_f32_e32 v22, v13, v20
	v_add_f32_e32 v23, v15, v1
	v_fmac_f32_e32 v11, 0xb102e308, v0
	v_sub_f32_e32 v0, v22, v13
	v_sub_f32_e32 v13, v23, v15
	v_rcp_f32_e32 v15, v23
	v_add_f32_e32 v24, v21, v11
	v_sub_f32_e32 v1, v1, v13
	v_sub_f32_e32 v13, v24, v21
	v_sub_f32_e32 v11, v11, v13
	v_mul_f32_e32 v13, v22, v15
	v_sub_f32_e32 v0, v20, v0
	v_mul_f32_e32 v20, v23, v13
	v_fma_f32 v21, v13, v23, -v20
	v_fmac_f32_e32 v21, v13, v1
	v_add_f32_e32 v25, v20, v21
	v_sub_f32_e32 v26, v22, v25
	v_sub_f32_e32 v20, v25, v20
	v_sub_f32_e32 v22, v22, v26
	v_sub_f32_e32 v20, v20, v21
	v_sub_f32_e32 v21, v22, v25
	v_add_f32_e32 v0, v0, v21
	v_add_f32_e32 v0, v20, v0
	v_add_f32_e32 v20, v26, v0
	v_mul_f32_e32 v21, v15, v20
	v_sub_f32_e32 v22, v26, v20
	v_mul_f32_e32 v25, v23, v21
	v_add_f32_e32 v0, v0, v22
	v_add_f32_e32 v22, v13, v21
	v_fma_f32 v23, v21, v23, -v25
	v_sub_f32_e32 v13, v22, v13
	v_fmac_f32_e32 v23, v21, v1
	v_sub_f32_e32 v1, v21, v13
	v_add_f32_e32 v13, v25, v23
	v_sub_f32_e32 v21, v13, v25
	v_sub_f32_e32 v25, v20, v13
	v_sub_f32_e32 v20, v20, v25
	v_sub_f32_e32 v13, v20, v13
	v_sub_f32_e32 v21, v21, v23
	v_add_f32_e32 v0, v0, v13
	v_add_f32_e32 v0, v21, v0
	v_add_f32_e32 v0, v25, v0
	v_mul_f32_e32 v0, v15, v0
	v_add_f32_e32 v0, v1, v0
	v_add_f32_e32 v1, v22, v0
	v_mul_f32_e32 v13, v1, v1
	v_fmamk_f32 v21, v13, 0x3e9b6dac, v250
	v_sub_f32_e32 v15, v1, v22
	v_ldexp_f32 v20, v1, 1
	v_mul_f32_e32 v1, v1, v13
	v_fmaak_f32 v13, v13, v21, 0x3f2aaada
	v_mul_f32_e32 v1, v1, v13
	v_add_f32_e32 v13, v20, v1
	v_sub_f32_e32 v0, v0, v15
	v_sub_f32_e32 v15, v13, v20
	v_ldexp_f32 v0, v0, 1
	v_sub_f32_e32 v1, v1, v15
	v_add_f32_e32 v0, v0, v1
	v_add_f32_e32 v1, v13, v0
	v_sub_f32_e32 v13, v1, v13
	v_add_f32_e32 v15, v24, v1
	v_sub_f32_e32 v0, v0, v13
	v_sub_f32_e32 v13, v15, v24
	v_sub_f32_e32 v20, v15, v13
	v_sub_f32_e32 v1, v1, v13
	v_add_f32_e32 v13, v11, v0
	v_sub_f32_e32 v20, v24, v20
	v_sub_f32_e32 v21, v13, v11
	v_add_f32_e32 v1, v1, v20
	v_sub_f32_e32 v20, v13, v21
	v_sub_f32_e32 v0, v0, v21
	v_sub_f32_e32 v11, v11, v20
	v_add_f32_e32 v1, v13, v1
	v_add_f32_e32 v0, v0, v11
	v_add_f32_e32 v11, v15, v1
	v_sub_f32_e32 v13, v11, v15
	v_sub_f32_e32 v1, v1, v13
	v_add_f32_e32 v0, v0, v1
	s_mov_b32 s12, 0x7f800000
	v_add_f32_e32 v0, v11, v0
	v_cmp_neq_f32_e32 vcc, s12, v7
	v_mov_b32_e32 v1, 0x7fc00000
	s_mov_b32 s12, 0x33800000
	v_cndmask_b32_e32 v0, v251, v0, vcc
	v_cmp_ngt_f32_e32 vcc, -1.0, v7
	s_nop 1
	v_cndmask_b32_e32 v0, v1, v0, vcc
	v_cmp_neq_f32_e32 vcc, -1.0, v7
	s_nop 1
	v_cndmask_b32_e32 v0, v230, v0, vcc
	v_cmp_lt_f32_e64 vcc, |v7|, s12
	s_nop 1
	v_cndmask_b32_e32 v0, v0, v7, vcc
	v_add_f32_e32 v20, v2, v0
	v_mul_f32_e64 v7, v20, -v9
	ds_bpermute_b32 v11, v134, v7
	v_readlane_b32 s12, v253, 43
	s_waitcnt lgkmcnt(0)
	v_fma_f32 v4, v20, -v9, v11
	v_readlane_b32 s13, v253, 44
	s_nop 1
	v_cndmask_b32_e64 v9, v4, v7, s[12:13]
	ds_bpermute_b32 v11, v135, v9
	v_readlane_b32 s12, v253, 47
	s_waitcnt lgkmcnt(0)
	v_add_f32_e32 v11, v9, v11
	v_readlane_b32 s13, v253, 48
	s_nop 1
	v_cndmask_b32_e64 v13, v11, v9, s[12:13]
	ds_bpermute_b32 v15, v136, v13
	v_readlane_b32 s12, v253, 49
	s_waitcnt lgkmcnt(0)
	v_add_f32_e32 v15, v13, v15
	v_readlane_b32 s13, v253, 50
	s_nop 1
	v_cndmask_b32_e64 v21, v15, v13, s[12:13]
	ds_bpermute_b32 v22, v137, v21
	v_readlane_b32 s12, v253, 45
	s_waitcnt lgkmcnt(0)
	v_add_f32_e32 v22, v21, v22
	v_readlane_b32 s13, v253, 46
	s_nop 1
	v_cndmask_b32_e64 v21, v22, v21, s[12:13]
	ds_bpermute_b32 v22, v138, v21
	v_readlane_b32 s12, v253, 51
	s_waitcnt lgkmcnt(0)
	v_add_f32_e32 v16, v21, v22
	v_readlane_b32 s13, v253, 52
	s_nop 1
	v_cndmask_b32_e64 v16, v16, v21, s[12:13]
	ds_bpermute_b32 v17, v139, v16
	v_readlane_b32 s12, v253, 55
	s_waitcnt lgkmcnt(0)
	v_add_f32_e32 v17, v16, v17
	v_readlane_b32 s13, v253, 56
	s_nop 1
	v_cndmask_b32_e64 v16, v17, v16, s[12:13]
	ds_write2st64_b32 v140, v16, v20 offset1:8
	s_waitcnt lgkmcnt(0)
	s_barrier
	s_waitcnt vmcnt(0)
	v_mov_b64_e32 v[44:45], v[56:57]
	v_mov_b64_e32 v[46:47], v[58:59]
	v_mov_b64_e32 v[40:41], v[60:61]
	v_mov_b64_e32 v[42:43], v[62:63]
	v_mov_b64_e32 v[36:37], v[64:65]
	v_mov_b64_e32 v[38:39], v[66:67]
	v_mov_b64_e32 v[32:33], v[68:69]
	v_mov_b64_e32 v[34:35], v[70:71]
	v_mov_b64_e32 v[28:29], v[72:73]
	v_mov_b64_e32 v[30:31], v[74:75]
	v_mov_b64_e32 v[24:25], v[76:77]
	v_mov_b64_e32 v[26:27], v[78:79]
	v_mov_b64_e32 v[20:21], v[80:81]
	v_mov_b64_e32 v[22:23], v[82:83]
	v_mov_b64_e32 v[16:17], v[84:85]
	v_mov_b64_e32 v[18:19], v[86:87]
	v_mov_b64_e32 v[12:13], v[88:89]
	v_mov_b64_e32 v[14:15], v[90:91]
	v_mov_b64_e32 v[8:9], v[92:93]
	v_mov_b64_e32 v[10:11], v[94:95]
	v_mov_b64_e32 v[4:5], v[96:97]
	v_mov_b64_e32 v[6:7], v[98:99]
	v_mov_b64_e32 v[0:1], v[100:101]
	v_mov_b64_e32 v[2:3], v[102:103]
	s_mov_b64 s[12:13], exec
	v_readlane_b32 s76, v253, 59
	v_readlane_b32 s77, v253, 60
	s_and_b64 s[76:77], s[12:13], s[76:77]
	s_xor_b64 vcc, s[76:77], s[12:13]
	s_mov_b64 exec, s[76:77]
	s_cbranch_execz .LBB0_647
	s_mov_b64 s[12:13], exec
	v_readlane_b32 s76, v253, 61
	v_readlane_b32 s77, v253, 62
	s_and_b64 s[76:77], s[12:13], s[76:77]
	s_xor_b64 s[12:13], s[76:77], s[12:13]
	s_mov_b64 exec, s[76:77]
	s_cbranch_execz .LBB0_644
	s_waitcnt vmcnt(11)
	ds_write_b128 v157, v[44:47] offset:22528
